# speedup vs baseline: 1.0180x; 1.0180x over previous
.LBB0_3:
	v_lshlrev_b64 v[36:37], 1, v[32:33]
	v_lshl_add_u64 v[38:39], s[4:5], 0, v[36:37]
	s_mov_b32 s4, 0x800000
	s_waitcnt vmcnt(4)
	v_cvt_pk_f16_f32 v28, v28, v29
	v_cvt_pk_f16_f32 v29, v30, v31
	v_cvt_pk_f16_f32 v31, v22, v23
	s_waitcnt vmcnt(2)
	v_cvt_pk_f16_f32 v22, v16, v17
	v_add_co_u32_e32 v16, vcc, s4, v38
	v_cvt_pk_f16_f32 v30, v20, v21
	s_nop 0
	v_addc_co_u32_e32 v17, vcc, 0, v39, vcc
	v_cvt_pk_f16_f32 v20, v24, v25
	v_cvt_pk_f16_f32 v21, v26, v27
	v_cvt_pk_f16_f32 v23, v18, v19
	s_waitcnt vmcnt(0)
	v_cvt_pk_f16_f32 v8, v8, v9
	v_cvt_pk_f16_f32 v9, v10, v11
	v_cvt_pk_f16_f32 v10, v4, v5
	v_cvt_pk_f16_f32 v11, v6, v7
	v_lshl_add_u64 v[4:5], s[6:7], 0, v[36:37]
	s_andn2_b64 vcc, exec, s[8:9]
	global_store_dwordx4 v[38:39], v[28:31], off sc1
	global_store_dwordx4 v[16:17], v[20:23], off sc1
	global_store_dwordx4 v[4:5], v[8:11], off sc1
	s_cbranch_vccnz .LBB0_5
	v_lshl_add_u64 v[4:5], v[32:33], 1, s[6:7]
	v_add_co_u32_e32 v4, vcc, 0x800000, v4
	v_cvt_pk_f16_f32 v0, v35, v1
	v_cvt_pk_f16_f32 v1, v2, v3
	v_cvt_pk_f16_f32 v2, v12, v13
	v_cvt_pk_f16_f32 v3, v14, v15
	v_addc_co_u32_e32 v5, vcc, 0, v5, vcc
	global_store_dwordx4 v[4:5], v[0:3], off sc1

.LBB1_15:
	s_cmp_gt_i32 s77, 7
	s_cselect_b64 s[52:53], -1, 0
	s_lshl_b32 s4, s77, 2
	s_add_i32 s78, s4, s66
	s_or_b32 s37, s4, s62
	s_lshr_b32 s4, s27, 8
	s_and_b32 s4, s4, 0x7ff8
	v_and_b32_e32 v147, 64, v198
	s_add_i32 s10, s4, s78
	s_lshr_b32 s4, s27, 6
	v_xor_b32_e32 v146, 16, v198
	v_add_u32_e32 v206, 64, v147
	s_and_b32 s4, s4, 0x7fe0
	v_cmp_lt_i32_e32 vcc, v146, v206
	s_add_i32 s54, s4, s37
	s_cmp_lt_i32 s77, 8
	v_cndmask_b32_e32 v146, v198, v146, vcc
	v_lshlrev_b32_e32 v201, 2, v146
	v_mul_f32_e32 v146, v127, v127
	v_mul_f32_e32 v147, v129, v129
	s_cselect_b64 s[6:7], -1, 0
	v_fmac_f32_e32 v146, v126, v126
	v_fmac_f32_e32 v147, v128, v128
	s_and_b64 s[4:5], s[6:7], exec
	v_add_f32_e32 v153, v146, v147
	v_pk_mul_f32 v[146:147], v[124:125], v[124:125]
	v_pk_mul_f32 v[148:149], v[122:123], v[122:123]
	s_cselect_b32 s9, s23, s25
	s_cselect_b32 s8, s22, s24
	v_and_b32_e32 v152, 0x7cf, v199
	v_mov_b32_e32 v150, v146
	v_mov_b32_e32 v151, v148
	v_mov_b32_e32 v148, v147
	global_load_dwordx4 v[138:141], v194, s[8:9] offset:16
	global_load_dwordx4 v[142:145], v194, s[8:9]
	global_load_dwordx4 v[130:133], v194, s[8:9] offset:144
	global_load_dwordx4 v[134:137], v194, s[8:9] offset:128
	v_pk_add_f32 v[146:147], v[150:151], v[148:149]
	v_lshlrev_b32_e32 v170, 7, v152
	v_add_f32_e32 v147, v153, v147
	v_lshl_add_u64 v[158:159], v[172:173], 0, v[170:171]
	v_lshl_add_u64 v[150:151], v[174:175], 0, v[170:171]
	v_add_f32_e32 v207, v146, v147
	global_load_dwordx4 v[146:149], v[150:151], off offset:16
	s_nop 0
	global_load_dwordx4 v[150:153], v[150:151], off
	s_nop 0
	global_load_dwordx4 v[154:157], v[158:159], off offset:16
	s_nop 0
	global_load_dwordx4 v[158:161], v[158:159], off
	v_pk_mul_f32 v[184:185], v[112:113], v[112:113]
	v_pk_mul_f32 v[202:203], v[110:111], v[110:111]
	v_mov_b32_e32 v204, v184
	v_mov_b32_e32 v205, v202
	v_mov_b32_e32 v202, v185
	v_pk_add_f32 v[184:185], v[204:205], v[202:203]
	v_pk_mul_f32 v[202:203], v[106:107], v[106:107]
	v_add_f32_e32 v170, v207, v185
	v_add_f32_e32 v170, v184, v170
	v_pk_mul_f32 v[184:185], v[108:109], v[108:109]
	v_mov_b32_e32 v205, v202
	v_mov_b32_e32 v204, v184
	v_mov_b32_e32 v202, v185
	v_pk_add_f32 v[184:185], v[204:205], v[202:203]
	v_cndmask_b32_e64 v200, 1.0, v197, s[6:7]
	v_add_f32_e32 v170, v185, v170
	v_add_f32_e32 v170, v184, v170
	ds_bpermute_b32 v184, v201, v170
	v_xor_b32_e32 v185, 32, v198
	v_cmp_lt_i32_e32 vcc, v185, v206
	s_cselect_b32 s55, s17, s19
	v_or_b32_e32 v229, 16, v199
	v_cndmask_b32_e32 v185, v198, v185, vcc
	v_lshlrev_b32_e32 v202, 2, v185
	s_waitcnt lgkmcnt(0)
	v_add_f32_e32 v170, v170, v184
	ds_bpermute_b32 v184, v202, v170
	s_waitcnt lgkmcnt(0)
	v_add_f32_e32 v170, v170, v184
	v_fmamk_f32 v170, v170, 0x3c800000, v195
	v_mul_f32_e32 v184, 0x4f800000, v170
	v_cmp_gt_f32_e32 vcc, s70, v170
	s_nop 1
	v_cndmask_b32_e32 v170, v170, v184, vcc
	v_sqrt_f32_e32 v184, v170
	s_nop 0
	v_add_u32_e32 v185, -1, v184
	v_fma_f32 v203, -v185, v184, v170
	v_cmp_ge_f32_e64 s[8:9], 0, v203
	v_add_u32_e32 v203, 1, v184
	s_nop 0
	v_cndmask_b32_e64 v185, v184, v185, s[8:9]
	v_fma_f32 v184, -v203, v184, v170
	v_cmp_lt_f32_e64 s[8:9], 0, v184
	s_nop 1
	v_cndmask_b32_e64 v184, v185, v203, s[8:9]
	v_mul_f32_e32 v185, 0x37800000, v184
	v_cndmask_b32_e32 v184, v184, v185, vcc
	v_cmp_class_f32_e32 vcc, v170, v196
	v_lshl_or_b32 v203, s10, 17, v187
	v_lshl_or_b32 v185, s54, 17, v188
	v_cndmask_b32_e32 v170, v184, v170, vcc
	v_div_scale_f32 v184, s[8:9], v170, v170, v200
	v_rcp_f32_e32 v204, v184
	s_cselect_b32 s54, s16, s18
	s_cselect_b32 s10, s72, 0x1000
	v_fma_f32 v205, -v184, v204, 1.0
	v_fmac_f32_e32 v204, v205, v204
	v_div_scale_f32 v205, vcc, v200, v170, v200
	v_mul_f32_e32 v206, v205, v204
	v_fma_f32 v207, -v184, v206, v205
	v_fmac_f32_e32 v206, v207, v204
	v_fma_f32 v184, -v184, v206, v205
	v_div_fmas_f32 v184, v184, v204, v206
	v_div_fixup_f32 v170, v184, v170, v200
	v_pk_mul_f32 v[216:217], v[106:107], v[170:171] op_sel_hi:[1,0]
	v_pk_mul_f32 v[210:211], v[122:123], v[170:171] op_sel_hi:[1,0]
	s_waitcnt vmcnt(0)
	v_pk_mul_f32 v[216:217], v[130:131], v[216:217]
	v_pk_mul_f32 v[210:211], v[138:139], v[210:211]
	v_pk_mul_f32 v[224:225], v[146:147], v[216:217]
	v_pk_mul_f32 v[212:213], v[110:111], v[170:171] op_sel_hi:[1,0]
	v_pk_fma_f32 v[224:225], v[154:155], v[210:211], v[224:225] neg_lo:[0,0,1] neg_hi:[0,0,1]
	v_pk_mul_f32 v[154:155], v[154:155], v[216:217]
	v_pk_mul_f32 v[214:215], v[112:113], v[170:171] op_sel_hi:[1,0]
	v_pk_mul_f32 v[218:219], v[108:109], v[170:171] op_sel_hi:[1,0]
	v_pk_fma_f32 v[154:155], v[146:147], v[210:211], v[154:155]
	v_lshlrev_b32_e32 v146, 6, v199
	v_pk_mul_f32 v[204:205], v[128:129], v[170:171] op_sel_hi:[1,0]
	v_pk_mul_f32 v[206:207], v[126:127], v[170:171] op_sel_hi:[1,0]
	v_pk_mul_f32 v[208:209], v[124:125], v[170:171] op_sel_hi:[1,0]
	v_pk_mul_f32 v[214:215], v[136:137], v[214:215]
	v_pk_mul_f32 v[212:213], v[134:135], v[212:213]
	v_pk_mul_f32 v[218:219], v[132:133], v[218:219]
	v_cndmask_b32_e64 v184, v203, v185, s[6:7]
	v_and_b32_e32 v228, 0x1f000, v146
	v_pk_mul_f32 v[206:207], v[142:143], v[206:207]
	v_pk_mul_f32 v[204:205], v[144:145], v[204:205]
	v_pk_mul_f32 v[208:209], v[140:141], v[208:209]
	v_pk_mul_f32 v[220:221], v[150:151], v[212:213]
	v_pk_mul_f32 v[222:223], v[152:153], v[214:215]
	v_pk_mul_f32 v[226:227], v[148:149], v[218:219]
	v_or3_b32 v146, v228, v189, v184
	v_pk_fma_f32 v[222:223], v[160:161], v[204:205], v[222:223] neg_lo:[0,0,1] neg_hi:[0,0,1]
	v_pk_fma_f32 v[220:221], v[158:159], v[206:207], v[220:221] neg_lo:[0,0,1] neg_hi:[0,0,1]
	v_pk_fma_f32 v[226:227], v[156:157], v[208:209], v[226:227] neg_lo:[0,0,1] neg_hi:[0,0,1]
	v_pk_mul_f32 v[158:159], v[158:159], v[212:213]
	v_pk_mul_f32 v[160:161], v[160:161], v[214:215]
	v_pk_mul_f32 v[156:157], v[156:157], v[218:219]
	v_ashrrev_i32_e32 v147, 31, v146
	v_pk_fma_f32 v[152:153], v[152:153], v[204:205], v[160:161]
	v_pk_fma_f32 v[150:151], v[150:151], v[206:207], v[158:159]
	v_pk_fma_f32 v[156:157], v[148:149], v[208:209], v[156:157]
	v_lshl_add_u64 v[158:159], v[146:147], 1, s[54:55]
	v_cvt_pk_f16_f32 v146, v220, v221
	v_cvt_pk_f16_f32 v147, v222, v223
	v_cvt_pk_f16_f32 v148, v224, v225
	v_cvt_pk_f16_f32 v149, v226, v227
	v_cvt_pk_f16_f32 v150, v150, v151
	v_cvt_pk_f16_f32 v151, v152, v153
	v_cvt_pk_f16_f32 v152, v154, v155
	v_cvt_pk_f16_f32 v153, v156, v157
	global_store_dwordx4 v[158:159], v[146:149], off sc1
	v_pk_mul_f32 v[204:205], v[96:97], v[96:97]
	v_pk_mul_f32 v[206:207], v[94:95], v[94:95]
	v_lshl_add_u64 v[146:147], v[158:159], 0, s[10:11]
	global_store_dwordx4 v[146:147], v[150:153], off sc1
	v_mul_f32_e32 v146, v119, v119
	v_mul_f32_e32 v147, v121, v121
	v_fmac_f32_e32 v146, v118, v118
	v_fmac_f32_e32 v147, v120, v120
	v_add_f32_e32 v153, v146, v147
	v_pk_mul_f32 v[146:147], v[116:117], v[116:117]
	v_pk_mul_f32 v[148:149], v[114:115], v[114:115]
	v_bitop3_b32 v152, v199, s73, 16 bitop3:0xc8
	v_mov_b32_e32 v150, v146
	v_mov_b32_e32 v151, v148
	v_mov_b32_e32 v148, v147
	v_pk_add_f32 v[146:147], v[150:151], v[148:149]
	v_lshlrev_b32_e32 v170, 7, v152
	v_add_f32_e32 v147, v153, v147
	v_lshl_add_u64 v[158:159], v[172:173], 0, v[170:171]
	v_lshl_add_u64 v[150:151], v[174:175], 0, v[170:171]
	v_add_f32_e32 v210, v146, v147
	global_load_dwordx4 v[146:149], v[150:151], off offset:16
	s_nop 0
	global_load_dwordx4 v[150:153], v[150:151], off
	s_nop 0
	global_load_dwordx4 v[154:157], v[158:159], off offset:16
	s_nop 0
	global_load_dwordx4 v[158:161], v[158:159], off
	v_mov_b32_e32 v208, v204
	v_mov_b32_e32 v209, v206
	v_mov_b32_e32 v206, v205
	v_pk_add_f32 v[204:205], v[208:209], v[206:207]
	v_pk_mul_f32 v[206:207], v[90:91], v[90:91]
	v_add_f32_e32 v170, v210, v205
	v_add_f32_e32 v170, v204, v170
	v_pk_mul_f32 v[204:205], v[92:93], v[92:93]
	v_mov_b32_e32 v209, v206
	v_mov_b32_e32 v208, v204
	v_mov_b32_e32 v206, v205
	v_pk_add_f32 v[204:205], v[208:209], v[206:207]
	s_nop 0
	v_add_f32_e32 v170, v205, v170
	v_add_f32_e32 v170, v204, v170
	ds_bpermute_b32 v204, v201, v170
	s_waitcnt lgkmcnt(0)
	v_add_f32_e32 v170, v170, v204
	ds_bpermute_b32 v204, v202, v170
	s_waitcnt lgkmcnt(0)
	v_add_f32_e32 v170, v170, v204
	v_fmamk_f32 v170, v170, 0x3c800000, v195
	v_mul_f32_e32 v204, 0x4f800000, v170
	v_cmp_gt_f32_e32 vcc, s70, v170
	s_nop 1
	v_cndmask_b32_e32 v170, v170, v204, vcc
	v_sqrt_f32_e32 v204, v170
	s_nop 0
	v_add_u32_e32 v205, -1, v204
	v_fma_f32 v206, -v205, v204, v170
	v_cmp_ge_f32_e64 s[8:9], 0, v206
	v_add_u32_e32 v206, 1, v204
	s_nop 0
	v_cndmask_b32_e64 v205, v204, v205, s[8:9]
	v_fma_f32 v204, -v206, v204, v170
	v_cmp_lt_f32_e64 s[8:9], 0, v204
	s_nop 1
	v_cndmask_b32_e64 v204, v205, v206, s[8:9]
	v_mul_f32_e32 v205, 0x37800000, v204
	v_cndmask_b32_e32 v204, v204, v205, vcc
	v_cmp_class_f32_e32 vcc, v170, v196
	s_nop 1
	v_cndmask_b32_e32 v170, v204, v170, vcc
	v_div_scale_f32 v204, s[8:9], v170, v170, v200
	v_rcp_f32_e32 v205, v204
	s_mov_b64 s[8:9], -1
	v_fma_f32 v206, -v204, v205, 1.0
	v_fmac_f32_e32 v205, v206, v205
	v_div_scale_f32 v206, vcc, v200, v170, v200
	v_mul_f32_e32 v207, v206, v205
	v_fma_f32 v208, -v204, v207, v206
	v_fmac_f32_e32 v207, v208, v205
	v_fma_f32 v204, -v204, v207, v206
	v_div_fmas_f32 v204, v204, v205, v207
	v_div_fixup_f32 v170, v204, v170, v200
	v_pk_mul_f32 v[216:217], v[90:91], v[170:171] op_sel_hi:[1,0]
	v_pk_mul_f32 v[210:211], v[114:115], v[170:171] op_sel_hi:[1,0]
	v_pk_mul_f32 v[216:217], v[130:131], v[216:217]
	v_pk_mul_f32 v[210:211], v[138:139], v[210:211]
	v_pk_mul_f32 v[212:213], v[94:95], v[170:171] op_sel_hi:[1,0]
	v_pk_mul_f32 v[214:215], v[96:97], v[170:171] op_sel_hi:[1,0]
	s_waitcnt vmcnt(3)
	v_pk_mul_f32 v[224:225], v[146:147], v[216:217]
	v_pk_mul_f32 v[218:219], v[92:93], v[170:171] op_sel_hi:[1,0]
	s_waitcnt vmcnt(1)
	v_pk_fma_f32 v[224:225], v[154:155], v[210:211], v[224:225] neg_lo:[0,0,1] neg_hi:[0,0,1]
	v_pk_mul_f32 v[154:155], v[154:155], v[216:217]
	v_pk_mul_f32 v[204:205], v[120:121], v[170:171] op_sel_hi:[1,0]
	v_pk_fma_f32 v[154:155], v[146:147], v[210:211], v[154:155]
	v_lshlrev_b32_e32 v146, 3, v229
	v_pk_mul_f32 v[206:207], v[118:119], v[170:171] op_sel_hi:[1,0]
	v_pk_mul_f32 v[208:209], v[116:117], v[170:171] op_sel_hi:[1,0]
	v_pk_mul_f32 v[214:215], v[136:137], v[214:215]
	v_pk_mul_f32 v[212:213], v[134:135], v[212:213]
	v_pk_mul_f32 v[218:219], v[132:133], v[218:219]
	v_and_b32_e32 v146, 0xf8, v146
	v_pk_mul_f32 v[206:207], v[142:143], v[206:207]
	v_pk_mul_f32 v[204:205], v[144:145], v[204:205]
	v_pk_mul_f32 v[208:209], v[140:141], v[208:209]
	v_pk_mul_f32 v[220:221], v[150:151], v[212:213]
	v_pk_mul_f32 v[222:223], v[152:153], v[214:215]
	v_pk_mul_f32 v[226:227], v[148:149], v[218:219]
	v_or3_b32 v146, v228, v146, v184
	s_waitcnt vmcnt(0)
	v_pk_fma_f32 v[222:223], v[160:161], v[204:205], v[222:223] neg_lo:[0,0,1] neg_hi:[0,0,1]
	v_pk_fma_f32 v[220:221], v[158:159], v[206:207], v[220:221] neg_lo:[0,0,1] neg_hi:[0,0,1]
	v_pk_fma_f32 v[226:227], v[156:157], v[208:209], v[226:227] neg_lo:[0,0,1] neg_hi:[0,0,1]
	v_pk_mul_f32 v[158:159], v[158:159], v[212:213]
	v_pk_mul_f32 v[160:161], v[160:161], v[214:215]
	v_pk_mul_f32 v[156:157], v[156:157], v[218:219]
	v_ashrrev_i32_e32 v147, 31, v146
	v_pk_fma_f32 v[152:153], v[152:153], v[204:205], v[160:161]
	v_pk_fma_f32 v[150:151], v[150:151], v[206:207], v[158:159]
	v_pk_fma_f32 v[156:157], v[148:149], v[208:209], v[156:157]
	v_lshl_add_u64 v[158:159], v[146:147], 1, s[54:55]
	v_cvt_pk_f16_f32 v146, v220, v221
	v_cvt_pk_f16_f32 v147, v222, v223
	v_cvt_pk_f16_f32 v148, v224, v225
	v_cvt_pk_f16_f32 v149, v226, v227
	v_bitop3_b32 v184, v199, s74, 32 bitop3:0xc8
	v_cvt_pk_f16_f32 v150, v150, v151
	v_cvt_pk_f16_f32 v151, v152, v153
	v_cvt_pk_f16_f32 v152, v154, v155
	v_cvt_pk_f16_f32 v153, v156, v157
	global_store_dwordx4 v[158:159], v[146:149], off sc1
	v_lshlrev_b32_e32 v170, 7, v184
	v_mul_f32_e32 v204, v105, v105
	v_lshl_add_u64 v[146:147], v[158:159], 0, s[10:11]
	global_store_dwordx4 v[146:147], v[150:153], off sc1
	v_lshl_add_u64 v[158:159], v[174:175], 0, v[170:171]
	v_fmac_f32_e32 v204, v104, v104
	v_lshl_add_u64 v[150:151], v[172:173], 0, v[170:171]
	global_load_dwordx4 v[146:149], v[150:151], off offset:16
	global_load_dwordx4 v[154:157], v[150:151], off
	s_nop 0
	global_load_dwordx4 v[150:153], v[158:159], off offset:16
	s_nop 0
	global_load_dwordx4 v[158:161], v[158:159], off
	v_mul_f32_e32 v170, v103, v103
	v_fmac_f32_e32 v170, v102, v102
	v_add_f32_e32 v170, v170, v204
	v_pk_mul_f32 v[204:205], v[100:101], v[100:101]
	v_pk_mul_f32 v[206:207], v[98:99], v[98:99]
	v_mov_b32_e32 v208, v204
	v_mov_b32_e32 v209, v206
	v_mov_b32_e32 v206, v205
	v_pk_add_f32 v[204:205], v[208:209], v[206:207]
	v_pk_mul_f32 v[206:207], v[78:79], v[78:79]
	v_add_f32_e32 v170, v170, v205
	v_add_f32_e32 v170, v204, v170
	v_pk_mul_f32 v[204:205], v[80:81], v[80:81]
	v_mov_b32_e32 v209, v206
	v_mov_b32_e32 v208, v204
	v_mov_b32_e32 v206, v205
	v_pk_add_f32 v[204:205], v[208:209], v[206:207]
	v_pk_mul_f32 v[206:207], v[74:75], v[74:75]
	v_add_f32_e32 v170, v170, v205
	v_add_f32_e32 v170, v204, v170
	v_pk_mul_f32 v[204:205], v[76:77], v[76:77]
	v_mov_b32_e32 v209, v206
	v_mov_b32_e32 v208, v204
	v_mov_b32_e32 v206, v205
	v_pk_add_f32 v[204:205], v[208:209], v[206:207]
	s_mov_b64 vcc, s[4:5]
	v_add_f32_e32 v170, v205, v170
	v_add_f32_e32 v170, v204, v170
	ds_bpermute_b32 v204, v201, v170
	v_lshlrev_b32_e32 v205, 6, v184
	s_waitcnt lgkmcnt(0)
	v_add_f32_e32 v170, v170, v204
	ds_bpermute_b32 v204, v202, v170
	s_cbranch_vccnz .LBB1_17
	v_or_b32_e32 v184, 32, v199
	v_lshlrev_b32_e32 v184, 3, v184
	v_and_b32_e32 v206, 0x1f000, v205
	v_and_b32_e32 v184, 0x178, v184
	v_or3_b32 v184, v206, v184, v203
	s_mov_b64 s[8:9], 0

.LBB1_20:
	s_waitcnt lgkmcnt(0)
	v_add_f32_e32 v170, v170, v204
	v_fmamk_f32 v170, v170, 0x3c800000, v195
	v_mul_f32_e32 v185, 0x4f800000, v170
	v_cmp_gt_f32_e32 vcc, s70, v170
	s_lshl_b32 s10, s56, 1
	v_add_u32_e32 v228, 0x80, v199
	v_cndmask_b32_e32 v170, v170, v185, vcc
	v_sqrt_f32_e32 v185, v170
	s_nop 0
	v_add_u32_e32 v204, -1, v185
	v_fma_f32 v206, -v204, v185, v170
	v_add_u32_e32 v205, 1, v185
	v_cmp_ge_f32_e64 s[4:5], 0, v206
	s_nop 1
	v_cndmask_b32_e64 v204, v185, v204, s[4:5]
	v_fma_f32 v185, -v205, v185, v170
	v_cmp_lt_f32_e64 s[4:5], 0, v185
	s_nop 1
	v_cndmask_b32_e64 v185, v204, v205, s[4:5]
	v_mul_f32_e32 v204, 0x37800000, v185
	v_cndmask_b32_e32 v185, v185, v204, vcc
	v_cmp_class_f32_e32 vcc, v170, v196
	s_nop 1
	v_cndmask_b32_e32 v170, v185, v170, vcc
	v_div_scale_f32 v185, s[4:5], v170, v170, v200
	v_rcp_f32_e32 v204, v185
	s_nop 0
	v_fma_f32 v205, -v185, v204, 1.0
	v_fmac_f32_e32 v204, v205, v204
	v_div_scale_f32 v205, vcc, v200, v170, v200
	v_mul_f32_e32 v206, v205, v204
	v_fma_f32 v207, -v185, v206, v205
	v_fmac_f32_e32 v206, v207, v204
	v_fma_f32 v185, -v185, v206, v205
	v_div_fmas_f32 v185, v185, v204, v206
	v_div_fixup_f32 v170, v185, v170, v200
	v_pk_mul_f32 v[212:213], v[78:79], v[170:171] op_sel_hi:[1,0]
	v_pk_mul_f32 v[214:215], v[80:81], v[170:171] op_sel_hi:[1,0]
	v_pk_mul_f32 v[216:217], v[74:75], v[170:171] op_sel_hi:[1,0]
	v_pk_mul_f32 v[218:219], v[76:77], v[170:171] op_sel_hi:[1,0]
	v_pk_mul_f32 v[204:205], v[104:105], v[170:171] op_sel_hi:[1,0]
	v_pk_mul_f32 v[206:207], v[102:103], v[170:171] op_sel_hi:[1,0]
	v_pk_mul_f32 v[208:209], v[100:101], v[170:171] op_sel_hi:[1,0]
	v_pk_mul_f32 v[210:211], v[98:99], v[170:171] op_sel_hi:[1,0]
	v_pk_mul_f32 v[214:215], v[136:137], v[214:215]
	v_pk_mul_f32 v[212:213], v[134:135], v[212:213]
	v_pk_mul_f32 v[218:219], v[132:133], v[218:219]
	v_pk_mul_f32 v[216:217], v[130:131], v[216:217]
	v_pk_mul_f32 v[206:207], v[142:143], v[206:207]
	v_pk_mul_f32 v[204:205], v[144:145], v[204:205]
	v_pk_mul_f32 v[210:211], v[138:139], v[210:211]
	v_pk_mul_f32 v[208:209], v[140:141], v[208:209]
	s_waitcnt vmcnt(0)
	v_pk_mul_f32 v[220:221], v[158:159], v[212:213]
	v_pk_mul_f32 v[222:223], v[160:161], v[214:215]
	v_pk_mul_f32 v[224:225], v[150:151], v[216:217]
	v_pk_mul_f32 v[226:227], v[152:153], v[218:219]
	v_pk_fma_f32 v[222:223], v[156:157], v[204:205], v[222:223] neg_lo:[0,0,1] neg_hi:[0,0,1]
	v_pk_fma_f32 v[220:221], v[154:155], v[206:207], v[220:221] neg_lo:[0,0,1] neg_hi:[0,0,1]
	v_pk_fma_f32 v[226:227], v[148:149], v[208:209], v[226:227] neg_lo:[0,0,1] neg_hi:[0,0,1]
	v_pk_fma_f32 v[224:225], v[146:147], v[210:211], v[224:225] neg_lo:[0,0,1] neg_hi:[0,0,1]
	v_pk_mul_f32 v[154:155], v[154:155], v[212:213]
	v_pk_mul_f32 v[156:157], v[156:157], v[214:215]
	v_pk_mul_f32 v[146:147], v[146:147], v[216:217]
	v_pk_mul_f32 v[148:149], v[148:149], v[218:219]
	v_ashrrev_i32_e32 v185, 31, v184
	v_pk_fma_f32 v[156:157], v[160:161], v[204:205], v[156:157]
	v_pk_fma_f32 v[154:155], v[158:159], v[206:207], v[154:155]
	v_pk_fma_f32 v[158:159], v[152:153], v[208:209], v[148:149]
	v_pk_fma_f32 v[152:153], v[150:151], v[210:211], v[146:147]
	v_lshl_add_u64 v[160:161], v[184:185], 1, s[8:9]
	v_cvt_pk_f16_f32 v146, v220, v221
	v_cvt_pk_f16_f32 v147, v222, v223
	v_cvt_pk_f16_f32 v148, v224, v225
	v_cvt_pk_f16_f32 v149, v226, v227
	v_cvt_pk_f16_f32 v150, v154, v155
	v_cvt_pk_f16_f32 v151, v156, v157
	v_cvt_pk_f16_f32 v152, v152, v153
	v_cvt_pk_f16_f32 v153, v158, v159
	global_store_dwordx4 v[160:161], v[146:149], off sc1
	v_bitop3_b32 v226, v199, s75, 48 bitop3:0xc8
	v_lshlrev_b32_e32 v170, 7, v226
	v_lshl_add_u64 v[146:147], v[160:161], 0, s[10:11]
	global_store_dwordx4 v[146:147], v[150:153], off sc1
	v_mul_f32_e32 v146, v87, v87
	v_mul_f32_e32 v147, v89, v89
	v_fmac_f32_e32 v146, v86, v86
	v_fmac_f32_e32 v147, v88, v88
	v_add_f32_e32 v152, v146, v147
	v_pk_mul_f32 v[146:147], v[84:85], v[84:85]
	v_pk_mul_f32 v[148:149], v[82:83], v[82:83]
	v_mov_b32_e32 v150, v146
	v_mov_b32_e32 v151, v148
	v_mov_b32_e32 v148, v147
	v_pk_add_f32 v[146:147], v[150:151], v[148:149]
	v_lshl_add_u64 v[158:159], v[172:173], 0, v[170:171]
	v_add_f32_e32 v147, v152, v147
	v_lshl_add_u64 v[150:151], v[174:175], 0, v[170:171]
	v_add_f32_e32 v208, v146, v147
	global_load_dwordx4 v[146:149], v[150:151], off offset:16
	s_nop 0
	global_load_dwordx4 v[150:153], v[150:151], off
	s_nop 0
	global_load_dwordx4 v[154:157], v[158:159], off offset:16
	s_nop 0
	global_load_dwordx4 v[158:161], v[158:159], off
	v_pk_mul_f32 v[184:185], v[72:73], v[72:73]
	v_pk_mul_f32 v[204:205], v[70:71], v[70:71]
	v_mov_b32_e32 v206, v184
	v_mov_b32_e32 v207, v204
	v_mov_b32_e32 v204, v185
	v_pk_add_f32 v[184:185], v[206:207], v[204:205]
	v_pk_mul_f32 v[204:205], v[66:67], v[66:67]
	v_add_f32_e32 v170, v208, v185
	v_add_f32_e32 v170, v184, v170
	v_pk_mul_f32 v[184:185], v[68:69], v[68:69]
	v_mov_b32_e32 v207, v204
	v_mov_b32_e32 v206, v184
	v_mov_b32_e32 v204, v185
	v_pk_add_f32 v[184:185], v[206:207], v[204:205]
	v_or_b32_e32 v227, 48, v199
	v_add_f32_e32 v170, v185, v170
	v_add_f32_e32 v170, v184, v170
	ds_bpermute_b32 v184, v201, v170
	s_waitcnt lgkmcnt(0)
	v_add_f32_e32 v170, v170, v184
	ds_bpermute_b32 v184, v202, v170
	s_waitcnt lgkmcnt(0)
	v_add_f32_e32 v170, v170, v184
	v_fmamk_f32 v170, v170, 0x3c800000, v195
	v_mul_f32_e32 v184, 0x4f800000, v170
	v_cmp_gt_f32_e32 vcc, s70, v170
	s_nop 1
	v_cndmask_b32_e32 v170, v170, v184, vcc
	v_sqrt_f32_e32 v184, v170
	s_nop 0
	v_add_u32_e32 v185, -1, v184
	v_fma_f32 v204, -v185, v184, v170
	v_cmp_ge_f32_e64 s[4:5], 0, v204
	v_add_u32_e32 v204, 1, v184
	s_nop 0
	v_cndmask_b32_e64 v185, v184, v185, s[4:5]
	v_fma_f32 v184, -v204, v184, v170
	v_cmp_lt_f32_e64 s[4:5], 0, v184
	s_nop 1
	v_cndmask_b32_e64 v184, v185, v204, s[4:5]
	v_mul_f32_e32 v185, 0x37800000, v184
	v_cndmask_b32_e32 v184, v184, v185, vcc
	v_cmp_class_f32_e32 vcc, v170, v196
	s_nop 1
	v_cndmask_b32_e32 v170, v184, v170, vcc
	v_div_scale_f32 v184, s[4:5], v170, v170, v200
	v_rcp_f32_e32 v185, v184
	s_nop 0
	v_fma_f32 v204, -v184, v185, 1.0
	v_fmac_f32_e32 v185, v204, v185
	v_div_scale_f32 v204, vcc, v200, v170, v200
	v_mul_f32_e32 v205, v204, v185
	v_fma_f32 v206, -v184, v205, v204
	v_fmac_f32_e32 v205, v206, v185
	v_fma_f32 v184, -v184, v205, v204
	v_div_fmas_f32 v184, v184, v185, v205
	v_div_fixup_f32 v170, v184, v170, v200
	v_pk_mul_f32 v[214:215], v[66:67], v[170:171] op_sel_hi:[1,0]
	v_pk_mul_f32 v[208:209], v[82:83], v[170:171] op_sel_hi:[1,0]
	v_pk_mul_f32 v[214:215], v[130:131], v[214:215]
	v_pk_mul_f32 v[208:209], v[138:139], v[208:209]
	s_waitcnt vmcnt(3)
	v_pk_mul_f32 v[222:223], v[146:147], v[214:215]
	v_pk_mul_f32 v[210:211], v[70:71], v[170:171] op_sel_hi:[1,0]
	s_waitcnt vmcnt(1)
	v_pk_fma_f32 v[222:223], v[154:155], v[208:209], v[222:223] neg_lo:[0,0,1] neg_hi:[0,0,1]
	v_pk_mul_f32 v[154:155], v[154:155], v[214:215]
	v_pk_mul_f32 v[212:213], v[72:73], v[170:171] op_sel_hi:[1,0]
	v_pk_mul_f32 v[216:217], v[68:69], v[170:171] op_sel_hi:[1,0]
	v_pk_fma_f32 v[154:155], v[146:147], v[208:209], v[154:155]
	v_lshlrev_b32_e32 v146, 6, v226
	v_lshlrev_b32_e32 v147, 3, v227
	v_pk_mul_f32 v[184:185], v[88:89], v[170:171] op_sel_hi:[1,0]
	v_pk_mul_f32 v[204:205], v[86:87], v[170:171] op_sel_hi:[1,0]
	v_pk_mul_f32 v[206:207], v[84:85], v[170:171] op_sel_hi:[1,0]
	v_pk_mul_f32 v[212:213], v[136:137], v[212:213]
	v_pk_mul_f32 v[210:211], v[134:135], v[210:211]
	v_pk_mul_f32 v[216:217], v[132:133], v[216:217]
	v_and_b32_e32 v146, s79, v146
	v_and_b32_e32 v147, s57, v147
	v_pk_mul_f32 v[204:205], v[142:143], v[204:205]
	v_pk_mul_f32 v[184:185], v[144:145], v[184:185]
	v_pk_mul_f32 v[206:207], v[140:141], v[206:207]
	v_pk_mul_f32 v[218:219], v[150:151], v[210:211]
	v_pk_mul_f32 v[220:221], v[152:153], v[212:213]
	v_pk_mul_f32 v[224:225], v[148:149], v[216:217]
	v_or3_b32 v146, v147, v203, v146
	s_waitcnt vmcnt(0)
	v_pk_fma_f32 v[220:221], v[160:161], v[184:185], v[220:221] neg_lo:[0,0,1] neg_hi:[0,0,1]
	v_pk_fma_f32 v[218:219], v[158:159], v[204:205], v[218:219] neg_lo:[0,0,1] neg_hi:[0,0,1]
	v_pk_fma_f32 v[224:225], v[156:157], v[206:207], v[224:225] neg_lo:[0,0,1] neg_hi:[0,0,1]
	v_pk_mul_f32 v[158:159], v[158:159], v[210:211]
	v_pk_mul_f32 v[160:161], v[160:161], v[212:213]
	v_pk_mul_f32 v[156:157], v[156:157], v[216:217]
	v_ashrrev_i32_e32 v147, 31, v146
	v_pk_fma_f32 v[152:153], v[152:153], v[184:185], v[160:161]
	v_pk_fma_f32 v[150:151], v[150:151], v[204:205], v[158:159]
	v_pk_fma_f32 v[156:157], v[148:149], v[206:207], v[156:157]
	v_lshl_add_u64 v[158:159], v[146:147], 1, s[8:9]
	v_cvt_pk_f16_f32 v146, v218, v219
	v_cvt_pk_f16_f32 v147, v220, v221
	v_cvt_pk_f16_f32 v148, v222, v223
	v_cvt_pk_f16_f32 v149, v224, v225
	v_cvt_pk_f16_f32 v150, v150, v151
	v_cvt_pk_f16_f32 v151, v152, v153
	v_cvt_pk_f16_f32 v152, v154, v155
	v_cvt_pk_f16_f32 v153, v156, v157
	global_store_dwordx4 v[158:159], v[146:149], off sc1
	v_pk_mul_f32 v[184:185], v[48:49], v[48:49]
	v_pk_mul_f32 v[204:205], v[46:47], v[46:47]
	v_lshl_add_u64 v[146:147], v[158:159], 0, s[10:11]
	global_store_dwordx4 v[146:147], v[150:153], off sc1
	v_mul_f32_e32 v146, v63, v63
	v_mul_f32_e32 v147, v65, v65
	v_fmac_f32_e32 v146, v62, v62
	v_fmac_f32_e32 v147, v64, v64
	v_add_f32_e32 v153, v146, v147
	v_pk_mul_f32 v[146:147], v[60:61], v[60:61]
	v_pk_mul_f32 v[148:149], v[58:59], v[58:59]
	v_and_b32_e32 v152, 0x7cf, v228
	v_mov_b32_e32 v150, v146
	v_mov_b32_e32 v151, v148
	v_mov_b32_e32 v148, v147
	v_pk_add_f32 v[146:147], v[150:151], v[148:149]
	v_lshlrev_b32_e32 v170, 7, v152
	v_add_f32_e32 v147, v153, v147
	v_lshl_add_u64 v[158:159], v[172:173], 0, v[170:171]
	v_lshl_add_u64 v[150:151], v[174:175], 0, v[170:171]
	v_add_f32_e32 v203, v146, v147
	global_load_dwordx4 v[146:149], v[150:151], off offset:16
	s_nop 0
	global_load_dwordx4 v[150:153], v[150:151], off
	s_nop 0
	global_load_dwordx4 v[154:157], v[158:159], off offset:16
	s_nop 0
	global_load_dwordx4 v[158:161], v[158:159], off
	v_mov_b32_e32 v206, v184
	v_mov_b32_e32 v207, v204
	v_mov_b32_e32 v204, v185
	v_pk_add_f32 v[184:185], v[206:207], v[204:205]
	v_pk_mul_f32 v[204:205], v[42:43], v[42:43]
	v_add_f32_e32 v170, v203, v185
	v_add_f32_e32 v170, v184, v170
	v_pk_mul_f32 v[184:185], v[44:45], v[44:45]
	v_mov_b32_e32 v207, v204
	v_mov_b32_e32 v206, v184
	v_mov_b32_e32 v204, v185
	v_pk_add_f32 v[184:185], v[206:207], v[204:205]
	s_nop 0
	v_add_f32_e32 v170, v185, v170
	v_add_f32_e32 v170, v184, v170
	ds_bpermute_b32 v184, v201, v170
	v_lshrrev_b32_e32 v185, 8, v228
	v_and_b32_e32 v185, 0x7ff8, v185
	v_add_u32_e32 v185, s78, v185
	v_lshl_or_b32 v203, v185, 17, v187
	s_waitcnt lgkmcnt(0)
	v_add_f32_e32 v170, v170, v184
	ds_bpermute_b32 v184, v202, v170
	v_lshrrev_b32_e32 v185, 6, v228
	v_and_b32_e32 v185, 0x7fe0, v185
	v_add_u32_e32 v185, s37, v185
	v_lshl_or_b32 v185, v185, 17, v188
	s_waitcnt lgkmcnt(0)
	v_add_f32_e32 v170, v170, v184
	v_fmamk_f32 v170, v170, 0x3c800000, v195
	v_mul_f32_e32 v184, 0x4f800000, v170
	v_cmp_gt_f32_e32 vcc, s70, v170
	s_nop 1
	v_cndmask_b32_e32 v170, v170, v184, vcc
	v_sqrt_f32_e32 v184, v170
	s_nop 0
	v_add_u32_e32 v204, -1, v184
	v_fma_f32 v205, -v204, v184, v170
	v_cmp_ge_f32_e64 s[4:5], 0, v205
	v_add_u32_e32 v205, 1, v184
	s_nop 0
	v_cndmask_b32_e64 v204, v184, v204, s[4:5]
	v_fma_f32 v184, -v205, v184, v170
	v_cmp_lt_f32_e64 s[4:5], 0, v184
	s_nop 1
	v_cndmask_b32_e64 v184, v204, v205, s[4:5]
	v_mul_f32_e32 v204, 0x37800000, v184
	v_cndmask_b32_e32 v184, v184, v204, vcc
	v_cmp_class_f32_e32 vcc, v170, v196
	s_nop 1
	v_cndmask_b32_e32 v170, v184, v170, vcc
	v_div_scale_f32 v184, s[4:5], v170, v170, v200
	v_rcp_f32_e32 v204, v184
	s_nop 0
	v_fma_f32 v205, -v184, v204, 1.0
	v_fmac_f32_e32 v204, v205, v204
	v_div_scale_f32 v205, vcc, v200, v170, v200
	v_mul_f32_e32 v206, v205, v204
	v_fma_f32 v207, -v184, v206, v205
	v_fmac_f32_e32 v206, v207, v204
	v_fma_f32 v184, -v184, v206, v205
	v_div_fmas_f32 v184, v184, v204, v206
	v_div_fixup_f32 v170, v184, v170, v200
	v_pk_mul_f32 v[216:217], v[42:43], v[170:171] op_sel_hi:[1,0]
	v_pk_mul_f32 v[210:211], v[58:59], v[170:171] op_sel_hi:[1,0]
	v_pk_mul_f32 v[216:217], v[130:131], v[216:217]
	v_pk_mul_f32 v[210:211], v[138:139], v[210:211]
	v_pk_mul_f32 v[212:213], v[46:47], v[170:171] op_sel_hi:[1,0]
	v_pk_mul_f32 v[214:215], v[48:49], v[170:171] op_sel_hi:[1,0]
	s_waitcnt vmcnt(3)
	v_pk_mul_f32 v[224:225], v[146:147], v[216:217]
	v_pk_mul_f32 v[218:219], v[44:45], v[170:171] op_sel_hi:[1,0]
	s_waitcnt vmcnt(1)
	v_pk_fma_f32 v[224:225], v[154:155], v[210:211], v[224:225] neg_lo:[0,0,1] neg_hi:[0,0,1]
	v_pk_mul_f32 v[154:155], v[154:155], v[216:217]
	v_pk_mul_f32 v[204:205], v[64:65], v[170:171] op_sel_hi:[1,0]
	v_pk_fma_f32 v[154:155], v[146:147], v[210:211], v[154:155]
	v_lshlrev_b32_e32 v146, 6, v228
	v_pk_mul_f32 v[206:207], v[62:63], v[170:171] op_sel_hi:[1,0]
	v_pk_mul_f32 v[208:209], v[60:61], v[170:171] op_sel_hi:[1,0]
	v_pk_mul_f32 v[214:215], v[136:137], v[214:215]
	v_pk_mul_f32 v[212:213], v[134:135], v[212:213]
	v_pk_mul_f32 v[218:219], v[132:133], v[218:219]
	v_cndmask_b32_e64 v184, v203, v185, s[6:7]
	v_and_b32_e32 v146, 0x1f000, v146
	v_pk_mul_f32 v[206:207], v[142:143], v[206:207]
	v_pk_mul_f32 v[204:205], v[144:145], v[204:205]
	v_pk_mul_f32 v[208:209], v[140:141], v[208:209]
	v_pk_mul_f32 v[220:221], v[150:151], v[212:213]
	v_pk_mul_f32 v[222:223], v[152:153], v[214:215]
	v_pk_mul_f32 v[226:227], v[148:149], v[218:219]
	v_or3_b32 v146, v146, v189, v184
	s_waitcnt vmcnt(0)
	v_pk_fma_f32 v[222:223], v[160:161], v[204:205], v[222:223] neg_lo:[0,0,1] neg_hi:[0,0,1]
	v_pk_fma_f32 v[220:221], v[158:159], v[206:207], v[220:221] neg_lo:[0,0,1] neg_hi:[0,0,1]
	v_pk_fma_f32 v[226:227], v[156:157], v[208:209], v[226:227] neg_lo:[0,0,1] neg_hi:[0,0,1]
	v_pk_mul_f32 v[158:159], v[158:159], v[212:213]
	v_pk_mul_f32 v[160:161], v[160:161], v[214:215]
	v_pk_mul_f32 v[156:157], v[156:157], v[218:219]
	v_ashrrev_i32_e32 v147, 31, v146
	v_pk_fma_f32 v[152:153], v[152:153], v[204:205], v[160:161]
	v_pk_fma_f32 v[150:151], v[150:151], v[206:207], v[158:159]
	v_pk_fma_f32 v[156:157], v[148:149], v[208:209], v[156:157]
	v_lshl_add_u64 v[158:159], v[146:147], 1, s[54:55]
	v_cvt_pk_f16_f32 v146, v220, v221
	v_cvt_pk_f16_f32 v147, v222, v223
	v_cvt_pk_f16_f32 v148, v224, v225
	v_cvt_pk_f16_f32 v149, v226, v227
	v_cvt_pk_f16_f32 v150, v150, v151
	v_cvt_pk_f16_f32 v151, v152, v153
	v_cvt_pk_f16_f32 v152, v154, v155
	v_cvt_pk_f16_f32 v153, v156, v157
	global_store_dwordx4 v[158:159], v[146:149], off sc1
	v_add_u32_e32 v228, 0x90, v199
	v_pk_mul_f32 v[204:205], v[32:33], v[32:33]
	v_lshl_add_u64 v[146:147], v[158:159], 0, s[10:11]
	global_store_dwordx4 v[146:147], v[150:153], off sc1
	v_mul_f32_e32 v146, v55, v55
	v_mul_f32_e32 v147, v57, v57
	v_fmac_f32_e32 v146, v54, v54
	v_fmac_f32_e32 v147, v56, v56
	v_add_f32_e32 v153, v146, v147
	v_pk_mul_f32 v[146:147], v[52:53], v[52:53]
	v_pk_mul_f32 v[148:149], v[50:51], v[50:51]
	v_and_b32_e32 v152, 0x7df, v228
	v_mov_b32_e32 v150, v146
	v_mov_b32_e32 v151, v148
	v_mov_b32_e32 v148, v147
	v_pk_add_f32 v[146:147], v[150:151], v[148:149]
	v_lshlrev_b32_e32 v170, 7, v152
	v_add_f32_e32 v147, v153, v147
	v_lshl_add_u64 v[158:159], v[172:173], 0, v[170:171]
	v_lshl_add_u64 v[150:151], v[174:175], 0, v[170:171]
	v_add_f32_e32 v210, v146, v147
	global_load_dwordx4 v[146:149], v[150:151], off offset:16
	s_nop 0
	global_load_dwordx4 v[150:153], v[150:151], off
	s_nop 0
	global_load_dwordx4 v[154:157], v[158:159], off offset:16
	s_nop 0
	global_load_dwordx4 v[158:161], v[158:159], off
	v_pk_mul_f32 v[206:207], v[30:31], v[30:31]
	v_mov_b32_e32 v208, v204
	v_mov_b32_e32 v209, v206
	v_mov_b32_e32 v206, v205
	v_pk_add_f32 v[204:205], v[208:209], v[206:207]
	v_pk_mul_f32 v[206:207], v[26:27], v[26:27]
	v_add_f32_e32 v170, v210, v205
	v_add_f32_e32 v170, v204, v170
	v_pk_mul_f32 v[204:205], v[28:29], v[28:29]
	v_mov_b32_e32 v209, v206
	v_mov_b32_e32 v208, v204
	v_mov_b32_e32 v206, v205
	v_pk_add_f32 v[204:205], v[208:209], v[206:207]
	s_nop 0
	v_add_f32_e32 v170, v205, v170
	v_add_f32_e32 v170, v204, v170
	ds_bpermute_b32 v204, v201, v170
	s_waitcnt lgkmcnt(0)
	v_add_f32_e32 v170, v170, v204
	ds_bpermute_b32 v204, v202, v170
	s_waitcnt lgkmcnt(0)
	v_add_f32_e32 v170, v170, v204
	v_fmamk_f32 v170, v170, 0x3c800000, v195
	v_mul_f32_e32 v204, 0x4f800000, v170
	v_cmp_gt_f32_e32 vcc, s70, v170
	s_nop 1
	v_cndmask_b32_e32 v170, v170, v204, vcc
	v_sqrt_f32_e32 v204, v170
	s_nop 0
	v_add_u32_e32 v205, -1, v204
	v_fma_f32 v206, -v205, v204, v170
	v_cmp_ge_f32_e64 s[4:5], 0, v206
	v_add_u32_e32 v206, 1, v204
	s_nop 0
	v_cndmask_b32_e64 v205, v204, v205, s[4:5]
	v_fma_f32 v204, -v206, v204, v170
	v_cmp_lt_f32_e64 s[4:5], 0, v204
	s_nop 1
	v_cndmask_b32_e64 v204, v205, v206, s[4:5]
	v_mul_f32_e32 v205, 0x37800000, v204
	v_cndmask_b32_e32 v204, v204, v205, vcc
	v_cmp_class_f32_e32 vcc, v170, v196
	s_nop 1
	v_cndmask_b32_e32 v170, v204, v170, vcc
	v_div_scale_f32 v204, s[4:5], v170, v170, v200
	v_rcp_f32_e32 v205, v204
	s_mov_b64 s[4:5], -1
	v_fma_f32 v206, -v204, v205, 1.0
	v_fmac_f32_e32 v205, v206, v205
	v_div_scale_f32 v206, vcc, v200, v170, v200
	v_mul_f32_e32 v207, v206, v205
	v_fma_f32 v208, -v204, v207, v206
	v_fmac_f32_e32 v207, v208, v205
	v_fma_f32 v204, -v204, v207, v206
	v_div_fmas_f32 v204, v204, v205, v207
	v_div_fixup_f32 v170, v204, v170, v200
	v_pk_mul_f32 v[216:217], v[26:27], v[170:171] op_sel_hi:[1,0]
	v_pk_mul_f32 v[210:211], v[50:51], v[170:171] op_sel_hi:[1,0]
	v_pk_mul_f32 v[216:217], v[130:131], v[216:217]
	v_pk_mul_f32 v[210:211], v[138:139], v[210:211]
	v_pk_mul_f32 v[214:215], v[32:33], v[170:171] op_sel_hi:[1,0]
	s_waitcnt vmcnt(3)
	v_pk_mul_f32 v[224:225], v[146:147], v[216:217]
	v_pk_mul_f32 v[204:205], v[56:57], v[170:171] op_sel_hi:[1,0]
	s_waitcnt vmcnt(1)
	v_pk_fma_f32 v[224:225], v[154:155], v[210:211], v[224:225] neg_lo:[0,0,1] neg_hi:[0,0,1]
	v_pk_mul_f32 v[154:155], v[154:155], v[216:217]
	v_pk_mul_f32 v[212:213], v[30:31], v[170:171] op_sel_hi:[1,0]
	v_pk_mul_f32 v[214:215], v[136:137], v[214:215]
	v_pk_mul_f32 v[218:219], v[28:29], v[170:171] op_sel_hi:[1,0]
	v_pk_fma_f32 v[154:155], v[146:147], v[210:211], v[154:155]
	v_lshlrev_b32_e32 v146, 6, v228
	v_lshlrev_b32_e32 v147, 3, v228
	v_pk_mul_f32 v[206:207], v[54:55], v[170:171] op_sel_hi:[1,0]
	v_pk_mul_f32 v[204:205], v[144:145], v[204:205]
	v_pk_mul_f32 v[208:209], v[52:53], v[170:171] op_sel_hi:[1,0]
	v_pk_mul_f32 v[212:213], v[134:135], v[212:213]
	v_pk_mul_f32 v[218:219], v[132:133], v[218:219]
	v_pk_mul_f32 v[222:223], v[152:153], v[214:215]
	v_and_b32_e32 v146, 0x1f000, v146
	v_and_b32_e32 v147, 0xf8, v147
	v_pk_mul_f32 v[206:207], v[142:143], v[206:207]
	v_pk_mul_f32 v[208:209], v[140:141], v[208:209]
	v_pk_mul_f32 v[220:221], v[150:151], v[212:213]
	s_waitcnt vmcnt(0)
	v_pk_fma_f32 v[222:223], v[160:161], v[204:205], v[222:223] neg_lo:[0,0,1] neg_hi:[0,0,1]
	v_pk_mul_f32 v[226:227], v[148:149], v[218:219]
	v_pk_mul_f32 v[160:161], v[160:161], v[214:215]
	v_or3_b32 v146, v146, v147, v184
	v_pk_fma_f32 v[220:221], v[158:159], v[206:207], v[220:221] neg_lo:[0,0,1] neg_hi:[0,0,1]
	v_pk_fma_f32 v[226:227], v[156:157], v[208:209], v[226:227] neg_lo:[0,0,1] neg_hi:[0,0,1]
	v_pk_mul_f32 v[158:159], v[158:159], v[212:213]
	v_pk_fma_f32 v[152:153], v[152:153], v[204:205], v[160:161]
	v_pk_mul_f32 v[156:157], v[156:157], v[218:219]
	v_ashrrev_i32_e32 v147, 31, v146
	v_add_u32_e32 v204, 0xa0, v199
	v_pk_fma_f32 v[150:151], v[150:151], v[206:207], v[158:159]
	v_pk_fma_f32 v[156:157], v[148:149], v[208:209], v[156:157]
	v_lshl_add_u64 v[158:159], v[146:147], 1, s[54:55]
	v_cvt_pk_f16_f32 v146, v220, v221
	v_cvt_pk_f16_f32 v147, v222, v223
	v_cvt_pk_f16_f32 v148, v224, v225
	v_cvt_pk_f16_f32 v149, v226, v227
	v_and_b32_e32 v184, 0x7ef, v204
	v_cvt_pk_f16_f32 v150, v150, v151
	v_cvt_pk_f16_f32 v151, v152, v153
	v_cvt_pk_f16_f32 v152, v154, v155
	v_cvt_pk_f16_f32 v153, v156, v157
	global_store_dwordx4 v[158:159], v[146:149], off sc1
	v_lshlrev_b32_e32 v170, 7, v184
	v_mul_f32_e32 v205, v41, v41
	v_lshl_add_u64 v[146:147], v[158:159], 0, s[10:11]
	global_store_dwordx4 v[146:147], v[150:153], off sc1
	v_lshl_add_u64 v[158:159], v[174:175], 0, v[170:171]
	v_pk_mul_f32 v[206:207], v[36:37], v[36:37]
	v_lshl_add_u64 v[150:151], v[172:173], 0, v[170:171]
	global_load_dwordx4 v[146:149], v[150:151], off offset:16
	global_load_dwordx4 v[154:157], v[150:151], off
	s_nop 0
	global_load_dwordx4 v[150:153], v[158:159], off offset:16
	s_nop 0
	global_load_dwordx4 v[158:161], v[158:159], off
	v_mul_f32_e32 v170, v39, v39
	v_pk_mul_f32 v[208:209], v[34:35], v[34:35]
	v_fmac_f32_e32 v170, v38, v38
	v_fmac_f32_e32 v205, v40, v40
	v_mov_b32_e32 v210, v206
	v_mov_b32_e32 v211, v208
	v_mov_b32_e32 v208, v207
	v_add_f32_e32 v170, v170, v205
	v_pk_add_f32 v[206:207], v[210:211], v[208:209]
	v_pk_mul_f32 v[208:209], v[14:15], v[14:15]
	v_add_f32_e32 v170, v170, v207
	v_add_f32_e32 v170, v206, v170
	v_pk_mul_f32 v[206:207], v[16:17], v[16:17]
	v_mov_b32_e32 v211, v208
	v_mov_b32_e32 v210, v206
	v_mov_b32_e32 v208, v207
	v_pk_add_f32 v[206:207], v[210:211], v[208:209]
	v_pk_mul_f32 v[208:209], v[10:11], v[10:11]
	v_add_f32_e32 v170, v170, v207
	v_add_f32_e32 v170, v206, v170
	v_pk_mul_f32 v[206:207], v[12:13], v[12:13]
	v_mov_b32_e32 v211, v208
	v_mov_b32_e32 v210, v206
	v_mov_b32_e32 v208, v207
	v_pk_add_f32 v[206:207], v[210:211], v[208:209]
	s_andn2_b64 vcc, exec, s[52:53]
	v_add_f32_e32 v170, v207, v170
	v_add_f32_e32 v170, v206, v170
	ds_bpermute_b32 v205, v201, v170
	v_lshlrev_b32_e32 v206, 6, v184
	s_waitcnt lgkmcnt(0)
	v_add_f32_e32 v170, v170, v205
	ds_bpermute_b32 v205, v202, v170
	s_cbranch_vccnz .LBB1_22
	v_lshlrev_b32_e32 v204, 3, v204
	v_and_b32_e32 v184, 0x1f000, v206
	v_and_b32_e32 v204, 0x178, v204
	v_or3_b32 v184, v184, v204, v203
	s_mov_b64 s[4:5], 0

.LBB1_25:
	s_waitcnt lgkmcnt(0)
	v_add_f32_e32 v170, v170, v205
	v_fmamk_f32 v170, v170, 0x3c800000, v195
	v_mul_f32_e32 v185, 0x4f800000, v170
	v_cmp_gt_f32_e32 vcc, s70, v170
	s_lshl_b32 s10, s8, 1
	s_nop 0
	v_cndmask_b32_e32 v170, v170, v185, vcc
	v_sqrt_f32_e32 v185, v170
	s_nop 0
	v_add_u32_e32 v204, -1, v185
	v_fma_f32 v206, -v204, v185, v170
	v_add_u32_e32 v205, 1, v185
	v_cmp_ge_f32_e64 s[4:5], 0, v206
	s_nop 1
	v_cndmask_b32_e64 v204, v185, v204, s[4:5]
	v_fma_f32 v185, -v205, v185, v170
	v_cmp_lt_f32_e64 s[4:5], 0, v185
	s_nop 1
	v_cndmask_b32_e64 v185, v204, v205, s[4:5]
	v_mul_f32_e32 v204, 0x37800000, v185
	v_cndmask_b32_e32 v185, v185, v204, vcc
	v_cmp_class_f32_e32 vcc, v170, v196
	s_nop 1
	v_cndmask_b32_e32 v170, v185, v170, vcc
	v_div_scale_f32 v185, s[4:5], v170, v170, v200
	v_rcp_f32_e32 v204, v185
	s_nop 0
	v_fma_f32 v205, -v185, v204, 1.0
	v_fmac_f32_e32 v204, v205, v204
	v_div_scale_f32 v205, vcc, v200, v170, v200
	v_mul_f32_e32 v206, v205, v204
	v_fma_f32 v207, -v185, v206, v205
	v_fmac_f32_e32 v206, v207, v204
	v_fma_f32 v185, -v185, v206, v205
	v_div_fmas_f32 v185, v185, v204, v206
	v_div_fixup_f32 v170, v185, v170, v200
	v_pk_mul_f32 v[212:213], v[14:15], v[170:171] op_sel_hi:[1,0]
	v_pk_mul_f32 v[214:215], v[16:17], v[170:171] op_sel_hi:[1,0]
	v_pk_mul_f32 v[216:217], v[10:11], v[170:171] op_sel_hi:[1,0]
	v_pk_mul_f32 v[218:219], v[12:13], v[170:171] op_sel_hi:[1,0]
	v_pk_mul_f32 v[204:205], v[40:41], v[170:171] op_sel_hi:[1,0]
	v_pk_mul_f32 v[206:207], v[38:39], v[170:171] op_sel_hi:[1,0]
	v_pk_mul_f32 v[208:209], v[36:37], v[170:171] op_sel_hi:[1,0]
	v_pk_mul_f32 v[210:211], v[34:35], v[170:171] op_sel_hi:[1,0]
	v_pk_mul_f32 v[214:215], v[136:137], v[214:215]
	v_pk_mul_f32 v[212:213], v[134:135], v[212:213]
	v_pk_mul_f32 v[218:219], v[132:133], v[218:219]
	v_pk_mul_f32 v[216:217], v[130:131], v[216:217]
	v_pk_mul_f32 v[206:207], v[142:143], v[206:207]
	v_pk_mul_f32 v[204:205], v[144:145], v[204:205]
	v_pk_mul_f32 v[210:211], v[138:139], v[210:211]
	v_pk_mul_f32 v[208:209], v[140:141], v[208:209]
	s_waitcnt vmcnt(0)
	v_pk_mul_f32 v[220:221], v[158:159], v[212:213]
	v_pk_mul_f32 v[222:223], v[160:161], v[214:215]
	v_pk_mul_f32 v[224:225], v[150:151], v[216:217]
	v_pk_mul_f32 v[226:227], v[152:153], v[218:219]
	v_pk_fma_f32 v[222:223], v[156:157], v[204:205], v[222:223] neg_lo:[0,0,1] neg_hi:[0,0,1]
	v_pk_fma_f32 v[220:221], v[154:155], v[206:207], v[220:221] neg_lo:[0,0,1] neg_hi:[0,0,1]
	v_pk_fma_f32 v[226:227], v[148:149], v[208:209], v[226:227] neg_lo:[0,0,1] neg_hi:[0,0,1]
	v_pk_fma_f32 v[224:225], v[146:147], v[210:211], v[224:225] neg_lo:[0,0,1] neg_hi:[0,0,1]
	v_pk_mul_f32 v[154:155], v[154:155], v[212:213]
	v_pk_mul_f32 v[156:157], v[156:157], v[214:215]
	v_pk_mul_f32 v[146:147], v[146:147], v[216:217]
	v_pk_mul_f32 v[148:149], v[148:149], v[218:219]
	v_ashrrev_i32_e32 v185, 31, v184
	v_pk_fma_f32 v[156:157], v[160:161], v[204:205], v[156:157]
	v_pk_fma_f32 v[154:155], v[158:159], v[206:207], v[154:155]
	v_pk_fma_f32 v[158:159], v[152:153], v[208:209], v[148:149]
	v_pk_fma_f32 v[152:153], v[150:151], v[210:211], v[146:147]
	v_lshl_add_u64 v[160:161], v[184:185], 1, s[6:7]
	v_cvt_pk_f16_f32 v146, v220, v221
	v_cvt_pk_f16_f32 v147, v222, v223
	v_cvt_pk_f16_f32 v148, v224, v225
	v_cvt_pk_f16_f32 v149, v226, v227
	v_cvt_pk_f16_f32 v150, v154, v155
	v_cvt_pk_f16_f32 v151, v156, v157
	v_cvt_pk_f16_f32 v152, v152, v153
	v_cvt_pk_f16_f32 v153, v158, v159
	global_store_dwordx4 v[160:161], v[146:149], off sc1
	v_add_u32_e32 v208, 0xb0, v199
	v_and_b32_e32 v209, 0x7ff, v208
	v_lshl_add_u64 v[146:147], v[160:161], 0, s[10:11]
	global_store_dwordx4 v[146:147], v[150:153], off sc1
	v_mul_f32_e32 v146, v23, v23
	v_mul_f32_e32 v147, v25, v25
	v_fmac_f32_e32 v146, v22, v22
	v_fmac_f32_e32 v147, v24, v24
	v_add_f32_e32 v152, v146, v147
	v_pk_mul_f32 v[146:147], v[20:21], v[20:21]
	v_pk_mul_f32 v[148:149], v[18:19], v[18:19]
	v_mov_b32_e32 v150, v146
	v_mov_b32_e32 v151, v148
	v_mov_b32_e32 v148, v147
	v_pk_add_f32 v[146:147], v[150:151], v[148:149]
	v_lshlrev_b32_e32 v170, 7, v209
	v_add_f32_e32 v147, v152, v147
	v_lshl_add_u64 v[158:159], v[172:173], 0, v[170:171]
	v_lshl_add_u64 v[150:151], v[174:175], 0, v[170:171]
	v_add_f32_e32 v210, v146, v147
	global_load_dwordx4 v[146:149], v[150:151], off offset:16
	s_nop 0
	global_load_dwordx4 v[150:153], v[150:151], off
	s_nop 0
	global_load_dwordx4 v[154:157], v[158:159], off offset:16
	s_nop 0
	global_load_dwordx4 v[158:161], v[158:159], off
	v_pk_mul_f32 v[184:185], v[8:9], v[8:9]
	v_pk_mul_f32 v[204:205], v[6:7], v[6:7]
	v_mov_b32_e32 v206, v184
	v_mov_b32_e32 v207, v204
	v_mov_b32_e32 v204, v185
	v_pk_add_f32 v[184:185], v[206:207], v[204:205]
	v_pk_mul_f32 v[204:205], v[2:3], v[2:3]
	v_add_f32_e32 v170, v210, v185
	v_add_f32_e32 v170, v184, v170
	v_pk_mul_f32 v[184:185], v[4:5], v[4:5]
	v_mov_b32_e32 v207, v204
	v_mov_b32_e32 v206, v184
	v_mov_b32_e32 v204, v185
	v_pk_add_f32 v[184:185], v[206:207], v[204:205]
	s_nop 0
	v_add_f32_e32 v170, v185, v170
	v_add_f32_e32 v170, v184, v170
	ds_bpermute_b32 v184, v201, v170
	s_waitcnt lgkmcnt(0)
	v_add_f32_e32 v170, v170, v184
	ds_bpermute_b32 v184, v202, v170
	s_waitcnt lgkmcnt(0)
	v_add_f32_e32 v170, v170, v184
	v_fmamk_f32 v170, v170, 0x3c800000, v195
	v_mul_f32_e32 v184, 0x4f800000, v170
	v_cmp_gt_f32_e32 vcc, s70, v170
	s_nop 1
	v_cndmask_b32_e32 v170, v170, v184, vcc
	v_sqrt_f32_e32 v184, v170
	s_nop 0
	v_add_u32_e32 v185, -1, v184
	v_fma_f32 v201, -v185, v184, v170
	v_cmp_ge_f32_e64 s[4:5], 0, v201
	v_add_u32_e32 v201, 1, v184
	s_nop 0
	v_cndmask_b32_e64 v185, v184, v185, s[4:5]
	v_fma_f32 v184, -v201, v184, v170
	v_cmp_lt_f32_e64 s[4:5], 0, v184
	s_nop 1
	v_cndmask_b32_e64 v184, v185, v201, s[4:5]
	v_mul_f32_e32 v185, 0x37800000, v184
	v_cndmask_b32_e32 v184, v184, v185, vcc
	v_cmp_class_f32_e32 vcc, v170, v196
	s_nop 1
	v_cndmask_b32_e32 v170, v184, v170, vcc
	v_div_scale_f32 v184, s[4:5], v170, v170, v200
	v_rcp_f32_e32 v185, v184
	s_nop 0
	v_fma_f32 v201, -v184, v185, 1.0
	v_fmac_f32_e32 v185, v201, v185
	v_div_scale_f32 v201, vcc, v200, v170, v200
	v_mul_f32_e32 v202, v201, v185
	v_fma_f32 v204, -v184, v202, v201
	v_fmac_f32_e32 v202, v204, v185
	v_fma_f32 v184, -v184, v202, v201
	v_div_fmas_f32 v184, v184, v185, v202
	v_div_fixup_f32 v170, v184, v170, v200
	v_pk_mul_f32 v[184:185], v[24:25], v[170:171] op_sel_hi:[1,0]
	v_pk_mul_f32 v[200:201], v[22:23], v[170:171] op_sel_hi:[1,0]
	v_pk_mul_f32 v[144:145], v[144:145], v[184:185]
	v_pk_mul_f32 v[184:185], v[20:21], v[170:171] op_sel_hi:[1,0]
	v_pk_mul_f32 v[142:143], v[142:143], v[200:201]
	v_pk_mul_f32 v[140:141], v[140:141], v[184:185]
	v_pk_mul_f32 v[184:185], v[6:7], v[170:171] op_sel_hi:[1,0]
	v_pk_mul_f32 v[200:201], v[18:19], v[170:171] op_sel_hi:[1,0]
	v_pk_mul_f32 v[134:135], v[134:135], v[184:185]
	v_pk_mul_f32 v[184:185], v[2:3], v[170:171] op_sel_hi:[1,0]
	v_pk_mul_f32 v[138:139], v[138:139], v[200:201]
	v_pk_mul_f32 v[130:131], v[130:131], v[184:185]
	v_pk_mul_f32 v[200:201], v[8:9], v[170:171] op_sel_hi:[1,0]
	s_waitcnt vmcnt(3)
	v_pk_mul_f32 v[204:205], v[146:147], v[130:131]
	s_waitcnt vmcnt(1)
	v_pk_mul_f32 v[130:131], v[154:155], v[130:131]
	v_pk_mul_f32 v[136:137], v[136:137], v[200:201]
	v_pk_mul_f32 v[200:201], v[4:5], v[170:171] op_sel_hi:[1,0]
	v_pk_fma_f32 v[204:205], v[154:155], v[138:139], v[204:205] neg_lo:[0,0,1] neg_hi:[0,0,1]
	v_pk_fma_f32 v[138:139], v[146:147], v[138:139], v[130:131]
	v_lshlrev_b32_e32 v130, 6, v209
	v_lshlrev_b32_e32 v131, 3, v208
	v_pk_mul_f32 v[132:133], v[132:133], v[200:201]
	v_and_b32_e32 v130, s37, v130
	v_and_b32_e32 v131, s9, v131
	v_pk_mul_f32 v[184:185], v[150:151], v[134:135]
	v_pk_mul_f32 v[200:201], v[152:153], v[136:137]
	v_pk_mul_f32 v[206:207], v[148:149], v[132:133]
	v_or3_b32 v130, v131, v203, v130
	s_waitcnt vmcnt(0)
	v_pk_fma_f32 v[200:201], v[160:161], v[144:145], v[200:201] neg_lo:[0,0,1] neg_hi:[0,0,1]
	v_pk_fma_f32 v[184:185], v[158:159], v[142:143], v[184:185] neg_lo:[0,0,1] neg_hi:[0,0,1]
	v_pk_fma_f32 v[206:207], v[156:157], v[140:141], v[206:207] neg_lo:[0,0,1] neg_hi:[0,0,1]
	v_pk_mul_f32 v[134:135], v[158:159], v[134:135]
	v_pk_mul_f32 v[136:137], v[160:161], v[136:137]
	v_pk_mul_f32 v[132:133], v[156:157], v[132:133]
	v_ashrrev_i32_e32 v131, 31, v130
	v_pk_fma_f32 v[136:137], v[152:153], v[144:145], v[136:137]
	v_pk_fma_f32 v[134:135], v[150:151], v[142:143], v[134:135]
	v_pk_fma_f32 v[140:141], v[148:149], v[140:141], v[132:133]
	v_lshl_add_u64 v[142:143], v[130:131], 1, s[6:7]
	v_cvt_pk_f16_f32 v130, v184, v185
	v_cvt_pk_f16_f32 v131, v200, v201
	v_cvt_pk_f16_f32 v132, v204, v205
	v_cvt_pk_f16_f32 v133, v206, v207
	v_cvt_pk_f16_f32 v134, v134, v135
	v_cvt_pk_f16_f32 v135, v136, v137
	v_cvt_pk_f16_f32 v136, v138, v139
	v_cvt_pk_f16_f32 v137, v140, v141
	global_store_dwordx4 v[142:143], v[130:133], off sc1
	s_nop 1
	v_lshl_add_u64 v[130:131], v[142:143], 0, s[10:11]
	global_store_dwordx4 v[130:131], v[134:137], off sc1
	s_branch .LBB1_14
.LBB1_26:
	s_lshl_b32 s4, s77, 2
	s_lshr_b32 s5, s27, 8
	s_add_i32 s4, s4, s67
	s_and_b32 s5, s5, 0x7ff8
	s_add_i32 s5, s5, s4
	s_lshl_b32 s6, s27, 6
	s_lshl_b32 s5, s5, 17
	s_and_b32 s6, s6, 0x1f000
	v_cvt_pk_f16_f32 v70, v70, v71
	v_cvt_pk_f16_f32 v71, v72, v73
	v_cvt_pk_f16_f32 v72, v66, v67
	v_add_u32_e32 v66, 0x80, v199
	s_or_b32 s5, s5, s6
	v_lshrrev_b32_e32 v67, 8, v66
	v_or_b32_e32 v130, s5, v190
	v_and_b32_e32 v67, 0x7ff8, v67
	v_lshlrev_b32_e32 v66, 6, v66
	v_ashrrev_i32_e32 v131, 31, v130
	v_add_lshl_u32 v67, v67, s4, 17
	v_and_b32_e32 v66, 0x1f000, v66
	v_lshl_add_u64 v[130:131], v[130:131], 1, s[20:21]
	v_or3_b32 v66, v67, v66, v190
	v_cvt_pk_f16_f32 v126, v126, v127
	v_cvt_pk_f16_f32 v127, v128, v129
	v_cvt_pk_f16_f32 v128, v122, v123
	v_add_co_u32_e32 v122, vcc, s71, v130
	v_ashrrev_i32_e32 v67, 31, v66
	s_nop 0
	v_addc_co_u32_e32 v123, vcc, 0, v131, vcc
	v_lshl_add_u64 v[66:67], v[66:67], 1, s[20:21]
	v_cvt_pk_f16_f32 v62, v62, v63
	v_cvt_pk_f16_f32 v63, v64, v65
	v_cvt_pk_f16_f32 v64, v58, v59
	v_add_co_u32_e32 v58, vcc, s71, v66
	v_cvt_pk_f16_f32 v129, v124, v125
	v_cvt_pk_f16_f32 v110, v110, v111
	v_cvt_pk_f16_f32 v111, v112, v113
	v_cvt_pk_f16_f32 v112, v106, v107
	v_cvt_pk_f16_f32 v113, v108, v109
	v_cvt_pk_f16_f32 v106, v118, v119
	v_cvt_pk_f16_f32 v107, v120, v121
	v_cvt_pk_f16_f32 v108, v114, v115
	v_cvt_pk_f16_f32 v109, v116, v117
	v_cvt_pk_f16_f32 v94, v94, v95
	v_cvt_pk_f16_f32 v95, v96, v97
	v_cvt_pk_f16_f32 v96, v90, v91
	v_cvt_pk_f16_f32 v97, v92, v93
	v_cvt_pk_f16_f32 v90, v102, v103
	v_cvt_pk_f16_f32 v91, v104, v105
	v_cvt_pk_f16_f32 v92, v98, v99
	v_cvt_pk_f16_f32 v93, v100, v101
	v_cvt_pk_f16_f32 v78, v78, v79
	v_cvt_pk_f16_f32 v79, v80, v81
	v_cvt_pk_f16_f32 v80, v74, v75
	v_cvt_pk_f16_f32 v81, v76, v77
	v_cvt_pk_f16_f32 v74, v86, v87
	v_cvt_pk_f16_f32 v75, v88, v89
	v_cvt_pk_f16_f32 v76, v82, v83
	v_cvt_pk_f16_f32 v77, v84, v85
	v_cvt_pk_f16_f32 v73, v68, v69
	v_cvt_pk_f16_f32 v65, v60, v61
	v_cvt_pk_f16_f32 v46, v46, v47
	v_cvt_pk_f16_f32 v47, v48, v49
	v_cvt_pk_f16_f32 v48, v42, v43
	v_cvt_pk_f16_f32 v49, v44, v45
	v_addc_co_u32_e32 v59, vcc, 0, v67, vcc
	v_cvt_pk_f16_f32 v42, v54, v55
	v_cvt_pk_f16_f32 v43, v56, v57
	v_cvt_pk_f16_f32 v44, v50, v51
	v_cvt_pk_f16_f32 v45, v52, v53
	v_cvt_pk_f16_f32 v30, v30, v31
	v_cvt_pk_f16_f32 v31, v32, v33
	v_cvt_pk_f16_f32 v32, v26, v27
	v_cvt_pk_f16_f32 v33, v28, v29
	v_cvt_pk_f16_f32 v26, v38, v39
	v_cvt_pk_f16_f32 v27, v40, v41
	v_cvt_pk_f16_f32 v28, v34, v35
	v_cvt_pk_f16_f32 v29, v36, v37
	v_cvt_pk_f16_f32 v14, v14, v15
	v_cvt_pk_f16_f32 v15, v16, v17
	v_cvt_pk_f16_f32 v16, v10, v11
	v_cvt_pk_f16_f32 v17, v12, v13
	v_cvt_pk_f16_f32 v10, v22, v23
	v_cvt_pk_f16_f32 v11, v24, v25
	v_cvt_pk_f16_f32 v12, v18, v19
	v_cvt_pk_f16_f32 v13, v20, v21
	v_cvt_pk_f16_f32 v6, v6, v7
	v_cvt_pk_f16_f32 v7, v8, v9
	v_cvt_pk_f16_f32 v8, v2, v3
	v_cvt_pk_f16_f32 v9, v4, v5
	global_store_dwordx4 v[130:131], v[126:129], off sc1
	global_store_dwordx4 v[122:123], v[110:113], off sc1
	global_store_dwordx4 v[130:131], v[106:109], off offset:1024 sc1
	global_store_dwordx4 v[122:123], v[94:97], off offset:1024 sc1
	global_store_dwordx4 v[130:131], v[90:93], off offset:2048 sc1
	global_store_dwordx4 v[122:123], v[78:81], off offset:2048 sc1
	global_store_dwordx4 v[130:131], v[74:77], off offset:3072 sc1
	global_store_dwordx4 v[122:123], v[70:73], off offset:3072 sc1
	global_store_dwordx4 v[66:67], v[62:65], off sc1
	global_store_dwordx4 v[58:59], v[46:49], off sc1
	global_store_dwordx4 v[66:67], v[42:45], off offset:1024 sc1
	global_store_dwordx4 v[58:59], v[30:33], off offset:1024 sc1
	global_store_dwordx4 v[66:67], v[26:29], off offset:2048 sc1
	global_store_dwordx4 v[58:59], v[14:17], off offset:2048 sc1
	global_store_dwordx4 v[66:67], v[10:13], off offset:3072 sc1
	global_store_dwordx4 v[58:59], v[6:9], off offset:3072 sc1
	s_andn2_b64 vcc, exec, s[0:1]
	s_mov_b64 s[0:1], -1
	s_cbranch_vccnz .LBB1_5

.LBB1_40:
	v_add_u32_e32 v2, s0, v18
	v_and_b32_e32 v20, 32, v19
	v_ashrrev_i32_e32 v21, 8, v19
	v_and_b32_e32 v22, 0x7c0, v16
	v_add_u32_e32 v23, s0, v14
	v_lshrrev_b32_e32 v34, 7, v2
	v_bitop3_b32 v20, v2, v20, 48 bitop3:0x6c
	v_and_b32_e32 v24, 32, v15
	v_ashrrev_i32_e32 v25, 8, v15
	v_lshrrev_b32_e32 v35, 5, v2
	v_lshrrev_b32_e32 v36, 9, v2
	v_bfe_u32 v37, v2, 6, 2
	v_and_b32_e32 v21, 0xffffff80, v21
	v_lshlrev_b32_e32 v2, 2, v22
	v_lshrrev_b32_e32 v22, 7, v23
	v_lshrrev_b32_e32 v20, 1, v20
	v_and_b32_e32 v34, 0x60, v34
	v_add_u32_e32 v26, s0, v10
	v_lshrrev_b32_e32 v38, 5, v23
	v_bitop3_b32 v24, v23, v24, 48 bitop3:0x6c
	v_lshrrev_b32_e32 v39, 9, v23
	v_bfe_u32 v23, v23, 6, 2
	v_and_b32_e32 v25, 0xffffff80, v25
	v_and_b32_e32 v47, 24, v35
	v_and_b32_e32 v36, 4, v36
	v_and_b32_e32 v22, 0x60, v22
	v_and_or_b32 v35, v35, 32, v20
	v_or3_b32 v20, v37, v21, v34
	v_and_b32_e32 v27, 32, v11
	v_ashrrev_i32_e32 v28, 8, v11
	v_lshrrev_b32_e32 v41, 7, v26
	v_and_b32_e32 v48, 24, v38
	v_and_b32_e32 v39, 4, v39
	v_or3_b32 v21, v23, v25, v22
	v_or3_b32 v20, v20, v36, v47
	v_add_u32_e32 v29, s0, v6
	v_lshrrev_b32_e32 v42, 5, v26
	v_bitop3_b32 v27, v26, v27, 48 bitop3:0x6c
	v_lshrrev_b32_e32 v43, 9, v26
	v_bfe_u32 v26, v26, 6, 2
	v_and_b32_e32 v28, 0xffffff80, v28
	v_and_b32_e32 v41, 0x60, v41
	v_or3_b32 v22, v21, v39, v48
	v_ashrrev_i32_e32 v21, 31, v20
	v_and_b32_e32 v30, 32, v7
	v_ashrrev_i32_e32 v31, 8, v7
	v_lshrrev_b32_e32 v44, 7, v29
	v_lshrrev_b32_e32 v24, 1, v24
	v_and_b32_e32 v49, 24, v42
	v_and_b32_e32 v43, 4, v43
	v_or3_b32 v23, v26, v28, v41
	v_lshlrev_b64 v[20:21], 13, v[20:21]
	v_lshrrev_b32_e32 v45, 5, v29
	v_bitop3_b32 v30, v29, v30, 48 bitop3:0x6c
	v_lshrrev_b32_e32 v46, 9, v29
	v_bfe_u32 v29, v29, 6, 2
	v_and_b32_e32 v31, 0xffffff80, v31
	v_and_b32_e32 v44, 0x60, v44
	v_and_or_b32 v34, v38, 32, v24
	v_or3_b32 v24, v23, v43, v49
	v_ashrrev_i32_e32 v23, 31, v22
	v_lshl_add_u64 v[20:21], s[38:39], 0, v[20:21]
	v_and_b32_e32 v32, 0x7c0, v12
	v_lshrrev_b32_e32 v30, 1, v30
	v_and_b32_e32 v50, 24, v45
	v_and_b32_e32 v46, 4, v46
	v_or3_b32 v25, v29, v31, v44
	v_lshlrev_b64 v[22:23], 13, v[22:23]
	v_lshl_add_u64 v[20:21], v[20:21], 0, v[2:3]
	v_lshlrev_b32_e32 v2, 2, v35
	v_and_or_b32 v51, v45, 32, v30
	v_or3_b32 v26, v25, v46, v50
	v_ashrrev_i32_e32 v25, 31, v24
	v_lshl_add_u64 v[28:29], s[38:39], 0, v[22:23]
	v_lshl_add_u64 v[30:31], v[20:21], 0, v[2:3]
	v_lshlrev_b32_e32 v2, 2, v32
	v_and_b32_e32 v33, 0x7c0, v8
	v_lshrrev_b32_e32 v27, 1, v27
	v_lshlrev_b64 v[24:25], 13, v[24:25]
	v_lshl_add_u64 v[28:29], v[28:29], 0, v[2:3]
	v_lshlrev_b32_e32 v2, 2, v34
	v_and_or_b32 v42, v42, 32, v27
	v_ashrrev_i32_e32 v27, 31, v26
	v_lshl_add_u64 v[36:37], s[38:39], 0, v[24:25]
	v_lshl_add_u64 v[38:39], v[28:29], 0, v[2:3]
	v_lshlrev_b32_e32 v2, 2, v33
	v_and_b32_e32 v40, 0x7c0, v0
	v_lshlrev_b64 v[26:27], 13, v[26:27]
	v_lshl_add_u64 v[36:37], v[36:37], 0, v[2:3]
	v_lshlrev_b32_e32 v2, 2, v42
	v_lshl_add_u64 v[44:45], s[38:39], 0, v[26:27]
	global_load_dwordx4 v[20:23], v[30:31], off nt
	global_load_dwordx4 v[24:27], v[30:31], off offset:16 nt
	v_lshl_add_u64 v[46:47], v[36:37], 0, v[2:3]
	v_lshlrev_b32_e32 v2, 2, v40
	global_load_dwordx4 v[28:31], v[38:39], off offset:16 nt
	global_load_dwordx4 v[32:35], v[38:39], off nt
	v_lshl_add_u64 v[44:45], v[44:45], 0, v[2:3]
	v_lshlrev_b32_e32 v2, 2, v51
	global_load_dwordx4 v[36:39], v[46:47], off nt
	global_load_dwordx4 v[40:43], v[46:47], off offset:16 nt
	v_lshl_add_u64 v[52:53], v[44:45], 0, v[2:3]
	global_load_dwordx4 v[44:47], v[52:53], off nt
	global_load_dwordx4 v[48:51], v[52:53], off offset:16 nt
	v_lshl_add_u64 v[52:53], v[4:5], 0, s[0:1]
	v_add_co_u32_e32 v54, vcc, s4, v52
	s_add_u32 s0, s0, 0x8000
	s_nop 0
	v_addc_co_u32_e32 v55, vcc, 0, v53, vcc
	v_add_co_u32_e32 v56, vcc, s5, v52
	s_addc_u32 s1, s1, 0
	s_nop 0
	v_addc_co_u32_e32 v57, vcc, 0, v53, vcc
	v_add_co_u32_e32 v58, vcc, s6, v52
	v_lshl_add_u64 v[0:1], v[0:1], 0, s[2:3]
	v_add_u32_e32 v7, 0x800, v7
	v_lshl_add_u64 v[8:9], v[8:9], 0, s[2:3]
	v_add_u32_e32 v11, 0x800, v11
	v_lshl_add_u64 v[12:13], v[12:13], 0, s[2:3]
	v_add_u32_e32 v15, 0x800, v15
	v_lshl_add_u64 v[16:17], v[16:17], 0, s[2:3]
	v_add_u32_e32 v19, 0x800, v19
	v_addc_co_u32_e32 v59, vcc, 0, v53, vcc
	s_cmp_eq_u32 s0, 0x20000
	s_waitcnt vmcnt(7)
	v_cvt_pk_f16_f32 v20, v20, v21
	v_cvt_pk_f16_f32 v21, v22, v23
	s_waitcnt vmcnt(6)
	v_cvt_pk_f16_f32 v22, v24, v25
	v_cvt_pk_f16_f32 v23, v26, v27
	global_store_dwordx4 v[52:53], v[20:23], off sc1
	s_waitcnt vmcnt(5)
	s_nop 0
	v_cvt_pk_f16_f32 v20, v32, v33
	v_cvt_pk_f16_f32 v21, v34, v35
	v_cvt_pk_f16_f32 v22, v28, v29
	v_cvt_pk_f16_f32 v23, v30, v31
	global_store_dwordx4 v[54:55], v[20:23], off sc1
	s_waitcnt vmcnt(5)
	s_nop 0
	v_cvt_pk_f16_f32 v20, v36, v37
	v_cvt_pk_f16_f32 v21, v38, v39
	s_waitcnt vmcnt(4)
	v_cvt_pk_f16_f32 v22, v40, v41
	v_cvt_pk_f16_f32 v23, v42, v43
	global_store_dwordx4 v[56:57], v[20:23], off sc1
	s_waitcnt vmcnt(4)
	s_nop 0
	v_cvt_pk_f16_f32 v20, v44, v45
	v_cvt_pk_f16_f32 v21, v46, v47
	s_waitcnt vmcnt(3)
	v_cvt_pk_f16_f32 v22, v48, v49
	v_cvt_pk_f16_f32 v23, v50, v51
	global_store_dwordx4 v[58:59], v[20:23], off sc1
	s_cbranch_scc0 .LBB1_40

.LBB3_1:
	s_or_b64 exec, exec, s[4:5]
	s_waitcnt lgkmcnt(0)
	v_add_u32_e32 v3, s55, v232
	ds_read_b128 v[4:7], v3 offset:49280
	ds_read_b128 v[8:11], v3 offset:49312
	s_lshl_b32 s4, s53, 12
	s_add_i32 s4, s4, 0
	s_mov_b64 s[30:31], 0
	s_waitcnt lgkmcnt(1)
	v_rcp_f32_e32 v12, v4
	v_rcp_f32_e32 v13, v5
	v_rcp_f32_e32 v14, v6
	v_rcp_f32_e32 v15, v7
	s_waitcnt lgkmcnt(0)
	v_rcp_f32_e32 v16, v8
	ds_read_b128 v[4:7], v3 offset:49344
	v_rcp_f32_e32 v17, v9
	v_rcp_f32_e32 v66, v10
	v_rcp_f32_e32 v67, v11
	ds_read_b128 v[8:11], v3 offset:49376
	s_waitcnt lgkmcnt(1)
	v_rcp_f32_e32 v3, v4
	v_rcp_f32_e32 v4, v5
	v_rcp_f32_e32 v5, v6
	v_rcp_f32_e32 v6, v7
	s_waitcnt lgkmcnt(0)
	v_rcp_f32_e32 v7, v8
	v_rcp_f32_e32 v8, v9
	v_rcp_f32_e32 v9, v10
	v_rcp_f32_e32 v10, v11
	v_lshlrev_b32_e32 v11, 1, v1
	v_add3_u32 v11, s4, v229, v11
	v_fma_mixlo_f16 v34, v34, v12, 0
	v_fma_mixlo_f16 v12, v50, v12, 0
	ds_write_b16 v11, v12 offset:51264
	v_fma_mixlo_f16 v12, v35, v13, 0
	ds_write_b16 v11, v12 offset:51328
	v_fma_mixlo_f16 v12, v51, v13, 0
	ds_write_b16 v11, v12 offset:51392
	v_fma_mixlo_f16 v12, v36, v14, 0
	ds_write_b16 v11, v12 offset:51456
	v_fma_mixlo_f16 v12, v52, v14, 0
	ds_write_b16 v11, v12 offset:51520
	v_fma_mixlo_f16 v12, v37, v15, 0
	ds_write_b16 v11, v12 offset:51584
	v_fma_mixlo_f16 v12, v53, v15, 0
	ds_write_b16 v11, v12 offset:51648
	v_fma_mixlo_f16 v12, v38, v16, 0
	ds_write_b16 v11, v12 offset:52224
	v_fma_mixlo_f16 v12, v54, v16, 0
	ds_write_b16 v11, v12 offset:52288
	v_fma_mixlo_f16 v12, v39, v17, 0
	ds_write_b16 v11, v12 offset:52352
	v_fma_mixlo_f16 v12, v55, v17, 0
	ds_write_b16 v11, v12 offset:52416
	v_fma_mixlo_f16 v12, v40, v66, 0
	ds_write_b16 v11, v12 offset:52480
	v_fma_mixlo_f16 v12, v56, v66, 0
	ds_write_b16 v11, v12 offset:52544
	v_fma_mixlo_f16 v12, v41, v67, 0
	ds_write_b16 v11, v12 offset:52608
	v_fma_mixlo_f16 v12, v57, v67, 0
	ds_write_b16 v11, v12 offset:52672
	v_fma_mixlo_f16 v12, v42, v3, 0
	v_fma_mixlo_f16 v3, v58, v3, 0
	ds_write_b16 v11, v3 offset:53312
	v_fma_mixlo_f16 v3, v43, v4, 0
	ds_write_b16 v11, v3 offset:53376
	v_fma_mixlo_f16 v3, v59, v4, 0
	ds_write_b16 v11, v3 offset:53440
	v_fma_mixlo_f16 v3, v44, v5, 0
	ds_write_b16 v11, v3 offset:53504
	v_fma_mixlo_f16 v3, v60, v5, 0
	ds_write_b16 v11, v3 offset:53568
	v_fma_mixlo_f16 v3, v45, v6, 0
	ds_write_b16 v11, v3 offset:53632
	v_fma_mixlo_f16 v3, v61, v6, 0
	ds_write_b16 v11, v3 offset:53696
	v_fma_mixlo_f16 v3, v46, v7, 0
	ds_write_b16 v11, v3 offset:54272
	v_fma_mixlo_f16 v3, v62, v7, 0
	ds_write_b16 v11, v3 offset:54336
	v_fma_mixlo_f16 v3, v47, v8, 0
	ds_write_b16 v11, v3 offset:54400
	v_fma_mixlo_f16 v3, v63, v8, 0
	ds_write_b16 v11, v3 offset:54464
	v_fma_mixlo_f16 v3, v48, v9, 0
	ds_write_b16 v11, v3 offset:54528
	v_fma_mixlo_f16 v3, v64, v9, 0
	ds_write_b16 v11, v3 offset:54592
	v_fma_mixlo_f16 v3, v49, v10, 0
	ds_write_b16 v11, v3 offset:54656
	v_fma_mixlo_f16 v3, v65, v10, 0
	ds_write_b16 v11, v3 offset:54720
	v_lshl_add_u32 v3, v233, 1, s4
	s_or_b32 s4, s54, s47
	s_ashr_i32 s4, s4, 2
	s_andn2_b32 s4, s4, 31
	s_add_i32 s4, s51, s4
	s_ashr_i32 s5, s4, 31
	ds_write_b16 v11, v34 offset:51200
	ds_write_b16 v11, v12 offset:53248
	s_lshl_b64 s[4:5], s[4:5], 14
	s_waitcnt lgkmcnt(0)
	s_add_u32 s4, s10, s4
	v_add_u32_e32 v8, v3, v235
	s_addc_u32 s5, s11, s5
	s_lshr_b32 s6, s52, 3
	ds_read_b128 v[4:7], v8 offset:51200
	v_and_or_b32 v9, s6, 12, v234
	v_lshlrev_b32_e32 v16, 9, v9
	v_or_b32_e32 v9, v236, v16
	v_lshlrev_b32_e32 v17, 1, v9
	s_waitcnt lgkmcnt(0)
	global_store_dwordx4 v17, v[4:7], s[4:5] sc1
	v_bitop3_b32 v12, v16, 16, v238 bitop3:0x36
	v_lshlrev_b32_e32 v34, 1, v12
	v_add_u32_e32 v4, v3, v237
	v_add_u32_e32 v3, v3, v239
	ds_read_b128 v[4:7], v4 offset:51200
	ds_read_b128 v[12:15], v3 offset:51200
	ds_read_b128 v[8:11], v8 offset:53248
	v_bitop3_b32 v3, v16, 16, v240 bitop3:0x36
	v_lshlrev_b32_e32 v3, 1, v3
	s_waitcnt lgkmcnt(2)
	global_store_dwordx4 v34, v[4:7], s[4:5] sc1
	s_waitcnt lgkmcnt(0)
	global_store_dwordx4 v17, v[8:11], s[4:5] offset:2048 sc1
	global_store_dwordx4 v3, v[12:15], s[4:5] sc1
	s_waitcnt lgkmcnt(0)
	s_barrier
	s_and_b64 vcc, exec, s[28:29]
	s_cbranch_vccnz .LBB3_104
